# out_kernel LDS layout: 128-byte rows with XOR swizzle (piece ^ ((row>>1)&7)) instead of the padded 144-byte stride, removing the 2-way ds_read_b128 bank conflicts
# speedup vs baseline: 1.0170x; 1.0170x over previous
_Z10out_kernelPKDF16_S0_PKfPf:
	s_load_dwordx8 s[4:11], s[0:1], 0x0
	s_lshr_b32 s12, s2, 3
	s_and_b32 s13, s2, 7
	s_lshl_b32 s14, s12, 5
	s_lshl_b32 s15, s13, 6
	v_lshrrev_b32_e32 v1, 3, v0
	v_and_b32_e32 v2, 7, v0
	v_lshlrev_b32_e32 v4, 4, v2
	v_add_u32_e32 v3, s14, v1
	v_lshl_or_b32 v3, v3, 10, v4
	v_add_u32_e32 v5, s15, v1
	v_lshl_or_b32 v5, v5, 10, v4
	v_add_u32_e32 v6, 0x8000, v5
	v_lshrrev_b32_e32 v7, 1, v1
	v_and_b32_e32 v7, 7, v7
	v_xor_b32_e32 v7, v7, v2
	v_lshlrev_b32_e32 v7, 4, v7
	v_lshl_add_u32 v7, v1, 7, v7
	v_and_b32_e32 v8, 15, v0
	v_and_b32_e32 v9, 48, v0
	v_lshrrev_b32_e32 v10, 6, v0
	v_lshrrev_b32_e32 v11, 1, v8
	v_and_b32_e32 v11, 7, v11
	v_lshlrev_b32_e32 v11, 4, v11
	v_xor_b32_e32 v11, v11, v9
	v_lshl_add_u32 v11, v8, 7, v11
	v_lshl_add_u32 v12, v10, 11, v11
	v_xor_b32_e32 v21, 64, v11
	v_xor_b32_e32 v22, 64, v12
	v_lshl_add_u32 v14, v10, 4, v8
	v_add_u32_e32 v14, s15, v14
	v_lshlrev_b32_e32 v15, 2, v14
	v_lshrrev_b32_e32 v13, 2, v9
	v_add_u32_e32 v13, s14, v13
	v_lshl_add_u32 v13, v13, 9, v14
	v_lshlrev_b32_e32 v16, 2, v13
	v_add_u32_e32 v17, 0x1000, v16
	v_add_u32_e32 v18, 0x8000, v16
	v_add_u32_e32 v19, 0x9000, v16
	s_waitcnt lgkmcnt(0)
	global_load_dwordx4 v[24:27], v3, s[4:5]
	global_load_dwordx4 v[28:31], v5, s[6:7]
	global_load_dwordx4 v[32:35], v6, s[6:7]
	global_load_dwordx4 v[36:39], v3, s[4:5] offset:128
	global_load_dwordx4 v[40:43], v5, s[6:7] offset:128
	global_load_dwordx4 v[44:47], v6, s[6:7] offset:128
	global_load_dwordx4 v[48:51], v3, s[4:5] offset:256
	global_load_dwordx4 v[52:55], v5, s[6:7] offset:256
	global_load_dwordx4 v[56:59], v6, s[6:7] offset:256
	global_load_dword v20, v15, s[8:9]
	s_waitcnt vmcnt(7)
	ds_write_b128 v7, v[24:27] offset:16384
	ds_write_b128 v7, v[28:31]
	ds_write_b128 v7, v[32:35] offset:4096
	global_load_dwordx4 v[24:27], v3, s[4:5] offset:384
	global_load_dwordx4 v[28:31], v5, s[6:7] offset:384
	global_load_dwordx4 v[32:35], v6, s[6:7] offset:384
	s_waitcnt lgkmcnt(0)
	s_barrier
	ds_read_b128 v[60:63], v11 offset:16384
	ds_read_b128 v[76:79], v12
	ds_read_b128 v[68:71], v11 offset:18432
	ds_read_b128 v[64:67], v21 offset:16384
	ds_read_b128 v[80:83], v22
	ds_read_b128 v[72:75], v21 offset:18432
	s_waitcnt vmcnt(7)
	ds_write_b128 v7, v[36:39] offset:20480
	ds_write_b128 v7, v[40:43] offset:8192
	ds_write_b128 v7, v[44:47] offset:12288
	global_load_dwordx4 v[36:39], v3, s[4:5] offset:512
	global_load_dwordx4 v[40:43], v5, s[6:7] offset:512
	global_load_dwordx4 v[44:47], v6, s[6:7] offset:512
	s_waitcnt lgkmcnt(7)
	v_mfma_f32_16x16x32_f16 a[0:3], v[60:63], v[76:79], 0
	s_waitcnt lgkmcnt(6)
	v_mfma_f32_16x16x32_f16 a[4:7], v[68:71], v[76:79], 0
	s_waitcnt lgkmcnt(4)
	v_mfma_f32_16x16x32_f16 a[0:3], v[64:67], v[80:83], a[0:3]
	s_waitcnt lgkmcnt(3)
	v_mfma_f32_16x16x32_f16 a[4:7], v[72:75], v[80:83], a[4:7]
	s_waitcnt lgkmcnt(0)
	s_barrier
	ds_read_b128 v[60:63], v11 offset:20480
	ds_read_b128 v[76:79], v12 offset:8192
	ds_read_b128 v[68:71], v11 offset:22528
	ds_read_b128 v[64:67], v21 offset:20480
	ds_read_b128 v[80:83], v22 offset:8192
	ds_read_b128 v[72:75], v21 offset:22528
	s_waitcnt vmcnt(7)
	ds_write_b128 v7, v[48:51] offset:16384
	ds_write_b128 v7, v[52:55]
	ds_write_b128 v7, v[56:59] offset:4096
	global_load_dwordx4 v[48:51], v3, s[4:5] offset:640
	global_load_dwordx4 v[52:55], v5, s[6:7] offset:640
	global_load_dwordx4 v[56:59], v6, s[6:7] offset:640
	s_waitcnt lgkmcnt(7)
	v_mfma_f32_16x16x32_f16 a[0:3], v[60:63], v[76:79], a[0:3]
	s_waitcnt lgkmcnt(6)
	v_mfma_f32_16x16x32_f16 a[4:7], v[68:71], v[76:79], a[4:7]
	s_waitcnt lgkmcnt(4)
	v_mfma_f32_16x16x32_f16 a[0:3], v[64:67], v[80:83], a[0:3]
	s_waitcnt lgkmcnt(3)
	v_mfma_f32_16x16x32_f16 a[4:7], v[72:75], v[80:83], a[4:7]
	s_waitcnt lgkmcnt(0)
	s_barrier
	ds_read_b128 v[60:63], v11 offset:16384
	ds_read_b128 v[76:79], v12
	ds_read_b128 v[68:71], v11 offset:18432
	ds_read_b128 v[64:67], v21 offset:16384
	ds_read_b128 v[80:83], v22
	ds_read_b128 v[72:75], v21 offset:18432
	s_waitcnt vmcnt(6)
	ds_write_b128 v7, v[24:27] offset:20480
	ds_write_b128 v7, v[28:31] offset:8192
	ds_write_b128 v7, v[32:35] offset:12288
	global_load_dwordx4 v[24:27], v3, s[4:5] offset:768
	global_load_dwordx4 v[28:31], v5, s[6:7] offset:768
	global_load_dwordx4 v[32:35], v6, s[6:7] offset:768
	s_waitcnt lgkmcnt(7)
	v_mfma_f32_16x16x32_f16 a[0:3], v[60:63], v[76:79], a[0:3]
	s_waitcnt lgkmcnt(6)
	v_mfma_f32_16x16x32_f16 a[4:7], v[68:71], v[76:79], a[4:7]
	s_waitcnt lgkmcnt(4)
	v_mfma_f32_16x16x32_f16 a[0:3], v[64:67], v[80:83], a[0:3]
	s_waitcnt lgkmcnt(3)
	v_mfma_f32_16x16x32_f16 a[4:7], v[72:75], v[80:83], a[4:7]
	s_waitcnt lgkmcnt(0)
	s_barrier
	ds_read_b128 v[60:63], v11 offset:20480
	ds_read_b128 v[76:79], v12 offset:8192
	ds_read_b128 v[68:71], v11 offset:22528
	ds_read_b128 v[64:67], v21 offset:20480
	ds_read_b128 v[80:83], v22 offset:8192
	ds_read_b128 v[72:75], v21 offset:22528
	s_waitcnt vmcnt(6)
	ds_write_b128 v7, v[36:39] offset:16384
	ds_write_b128 v7, v[40:43]
	ds_write_b128 v7, v[44:47] offset:4096
	global_load_dwordx4 v[36:39], v3, s[4:5] offset:896
	global_load_dwordx4 v[40:43], v5, s[6:7] offset:896
	global_load_dwordx4 v[44:47], v6, s[6:7] offset:896
	s_waitcnt lgkmcnt(7)
	v_mfma_f32_16x16x32_f16 a[0:3], v[60:63], v[76:79], a[0:3]
	s_waitcnt lgkmcnt(6)
	v_mfma_f32_16x16x32_f16 a[4:7], v[68:71], v[76:79], a[4:7]
	s_waitcnt lgkmcnt(4)
	v_mfma_f32_16x16x32_f16 a[0:3], v[64:67], v[80:83], a[0:3]
	s_waitcnt lgkmcnt(3)
	v_mfma_f32_16x16x32_f16 a[4:7], v[72:75], v[80:83], a[4:7]
	s_waitcnt lgkmcnt(0)
	s_barrier
	ds_read_b128 v[60:63], v11 offset:16384
	ds_read_b128 v[76:79], v12
	ds_read_b128 v[68:71], v11 offset:18432
	ds_read_b128 v[64:67], v21 offset:16384
	ds_read_b128 v[80:83], v22
	ds_read_b128 v[72:75], v21 offset:18432
	s_waitcnt vmcnt(6)
	ds_write_b128 v7, v[48:51] offset:20480
	ds_write_b128 v7, v[52:55] offset:8192
	ds_write_b128 v7, v[56:59] offset:12288
	s_waitcnt lgkmcnt(7)
	v_mfma_f32_16x16x32_f16 a[0:3], v[60:63], v[76:79], a[0:3]
	s_waitcnt lgkmcnt(6)
	v_mfma_f32_16x16x32_f16 a[4:7], v[68:71], v[76:79], a[4:7]
	s_waitcnt lgkmcnt(4)
	v_mfma_f32_16x16x32_f16 a[0:3], v[64:67], v[80:83], a[0:3]
	s_waitcnt lgkmcnt(3)
	v_mfma_f32_16x16x32_f16 a[4:7], v[72:75], v[80:83], a[4:7]
	s_waitcnt lgkmcnt(0)
	s_barrier
	ds_read_b128 v[60:63], v11 offset:20480
	ds_read_b128 v[76:79], v12 offset:8192
	ds_read_b128 v[68:71], v11 offset:22528
	ds_read_b128 v[64:67], v21 offset:20480
	ds_read_b128 v[80:83], v22 offset:8192
	ds_read_b128 v[72:75], v21 offset:22528
	s_waitcnt vmcnt(3)
	ds_write_b128 v7, v[24:27] offset:16384
	ds_write_b128 v7, v[28:31]
	ds_write_b128 v7, v[32:35] offset:4096
	s_waitcnt lgkmcnt(7)
	v_mfma_f32_16x16x32_f16 a[0:3], v[60:63], v[76:79], a[0:3]
	s_waitcnt lgkmcnt(6)
	v_mfma_f32_16x16x32_f16 a[4:7], v[68:71], v[76:79], a[4:7]
	s_waitcnt lgkmcnt(4)
	v_mfma_f32_16x16x32_f16 a[0:3], v[64:67], v[80:83], a[0:3]
	s_waitcnt lgkmcnt(3)
	v_mfma_f32_16x16x32_f16 a[4:7], v[72:75], v[80:83], a[4:7]
	s_waitcnt lgkmcnt(0)
	s_barrier
	ds_read_b128 v[60:63], v11 offset:16384
	ds_read_b128 v[76:79], v12
	ds_read_b128 v[68:71], v11 offset:18432
	ds_read_b128 v[64:67], v21 offset:16384
	ds_read_b128 v[80:83], v22
	ds_read_b128 v[72:75], v21 offset:18432
	s_waitcnt vmcnt(0)
	ds_write_b128 v7, v[36:39] offset:20480
	ds_write_b128 v7, v[40:43] offset:8192
	ds_write_b128 v7, v[44:47] offset:12288
	s_waitcnt lgkmcnt(7)
	v_mfma_f32_16x16x32_f16 a[0:3], v[60:63], v[76:79], a[0:3]
	s_waitcnt lgkmcnt(6)
	v_mfma_f32_16x16x32_f16 a[4:7], v[68:71], v[76:79], a[4:7]
	s_waitcnt lgkmcnt(4)
	v_mfma_f32_16x16x32_f16 a[0:3], v[64:67], v[80:83], a[0:3]
	s_waitcnt lgkmcnt(3)
	v_mfma_f32_16x16x32_f16 a[4:7], v[72:75], v[80:83], a[4:7]
	s_waitcnt lgkmcnt(0)
	s_barrier
	ds_read_b128 v[60:63], v11 offset:20480
	ds_read_b128 v[76:79], v12 offset:8192
	ds_read_b128 v[68:71], v11 offset:22528
	ds_read_b128 v[64:67], v21 offset:20480
	ds_read_b128 v[80:83], v22 offset:8192
	ds_read_b128 v[72:75], v21 offset:22528
	s_waitcnt lgkmcnt(4)
	v_mfma_f32_16x16x32_f16 a[0:3], v[60:63], v[76:79], a[0:3]
	s_waitcnt lgkmcnt(3)
	v_mfma_f32_16x16x32_f16 a[4:7], v[68:71], v[76:79], a[4:7]
	s_waitcnt lgkmcnt(1)
	v_mfma_f32_16x16x32_f16 a[0:3], v[64:67], v[80:83], a[0:3]
	s_waitcnt lgkmcnt(0)
	v_mfma_f32_16x16x32_f16 a[4:7], v[72:75], v[80:83], a[4:7]
	s_nop 7
	v_accvgpr_read_b32 v60, a0
	v_accvgpr_read_b32 v61, a1
	v_accvgpr_read_b32 v62, a2
	v_accvgpr_read_b32 v63, a3
	v_accvgpr_read_b32 v64, a4
	v_accvgpr_read_b32 v65, a5
	v_accvgpr_read_b32 v66, a6
	v_accvgpr_read_b32 v67, a7
	v_add_f32_e32 v60, v20, v60
	v_add_f32_e32 v61, v20, v61
	v_add_f32_e32 v62, v20, v62
	v_add_f32_e32 v63, v20, v63
	v_add_f32_e32 v64, v20, v64
	v_add_f32_e32 v65, v20, v65
	v_add_f32_e32 v66, v20, v66
	v_add_f32_e32 v67, v20, v67
	global_store_dword v16, v60, s[10:11]
	global_store_dword v16, v61, s[10:11] offset:2048
	global_store_dword v17, v62, s[10:11]
	global_store_dword v17, v63, s[10:11] offset:2048
	global_store_dword v18, v64, s[10:11]
	global_store_dword v18, v65, s[10:11] offset:2048
	global_store_dword v19, v66, s[10:11]
	global_store_dword v19, v67, s[10:11] offset:2048
	s_endpgm
